# GLA pass 2 chunk loop: waits no longer cover O-tile store acks (vmcnt 11->15 at loop top, 1->2 before second gate tile)
# speedup vs baseline: 1.0773x; 1.0021x over previous
; #define LAS __attribute__((address_space(3)))
; #define GLA_FENCE() asm volatile("" ::: "memory")
; template <int PASS> ...
;     ...
; #pragma unroll 1
;     for (int c = 0; c < CPP; ++c) {
;         const int tok0 = tokbase + c * CHK;
;         bf16x8 vb[2]; v4u gpre[2];
;         if (PASS == 2) GTP_BEGIN(24);
; #pragma unroll
;         for (int kt = 0; kt < 2; ++kt) vb[kt] = cat4(trread(vtr + kt * 32 * VS), trread(vtr + kt * 32 * VS + 4 * VS));
;         if (PASS == 2) {
;             const int it = w >> 1, jt0 = 2 * (w & 1);
;             f32x4 pa0 = (f32x4){0.f, 0.f, 0.f, 0.f}, pa1 = pa0;
;             bf16x8 fb[4], fa0[4], fa1[4];
;     ...
;             P_LOAD(0, 0); P_LOAD(1, 1); P_LOAD(2, 2);
; #pragma unroll
;             for (int ks = 0; ks < 8; ++ks) { if (ks + 3 < 8) P_LOAD((ks + 3) & 3, ks + 3); GLA_FENCE();
;                 pa0 = __builtin_amdgcn_mfma_f32_16x16x32_bf16(fa0[ks & 3], fb[ks & 3], pa0, 0, 0, 0); pa1 = __builtin_amdgcn_mfma_f32_16x16x32_bf16(fa1[ks & 3], fb[ks & 3], pa1, 0, 0, 0); }
;     ...
;             { const int i = 16 * it + r, j0 = 16 * jt0 + 4 * q; v2u o;
;               o.x = cvtpk(j0 + 0 <= i ? pa0[0] : 0.f, j0 + 1 <= i ? pa0[1] : 0.f); o.y = cvtpk(j0 + 2 <= i ? pa0[2] : 0.f, j0 + 3 <= i ? pa0[3] : 0.f);
;               *(LAS v2u*)(lds + OFF_P + i * PS + j0 * 2) = o;
;               o.x = cvtpk(j0 + 16 <= i ? pa1[0] : 0.f, j0 + 17 <= i ? pa1[1] : 0.f); o.y = cvtpk(j0 + 18 <= i ? pa1[2] : 0.f, j0 + 19 <= i ? pa1[3] : 0.f);
;               *(LAS v2u*)(lds + OFF_P + i * PS + (j0 + 16) * 2) = o; }
;             f32x4 Oa[4];
; #pragma unroll
;             for (int i4 = 0; i4 < 4; ++i4) Oa[i4] = (f32x4){0.f, 0.f, 0.f, 0.f};
;             bf16x8 qa[2][4];
;     ...
;             Q_LOAD(0, 0); GLA_FENCE();
; #pragma unroll
;             for (int ks = 0; ks < 8; ++ks) {
;                 if (ks + 1 < 8) Q_LOAD((ks + 1) & 1, ks + 1);
;                 GLA_FENCE();
;                 v4u bw; bw.x = cvtpk(S[2 * ks][0], S[2 * ks][1]); bw.y = cvtpk(S[2 * ks][2], S[2 * ks][3]); bw.z = cvtpk(S[2 * ks + 1][0], S[2 * ks + 1][1]); bw.w = cvtpk(S[2 * ks + 1][2], S[2 * ks + 1][3]);
;                 const bf16x8 bfrag = __builtin_bit_cast(bf16x8, bw);
; #pragma unroll
;                 for (int i4 = 0; i4 < 4; ++i4) Oa[i4] = __builtin_amdgcn_mfma_f32_16x16x32_bf16(bfrag, qa[ks & 1][i4], Oa[i4], 0, 0, 0);
;             }
.LBB0_424:
	v_add_u32_e32 v170, s73, v222
	ds_read_b64_tr_b16 v[106:107], v187
	ds_read_b64_tr_b16 v[108:109], v187 offset:1152
	ds_read_b64_tr_b16 v[110:111], v187 offset:9216
	ds_read_b64_tr_b16 v[112:113], v187 offset:10368
	s_waitcnt vmcnt(15)
	ds_read_b128 v[114:117], v170
	ds_read_b128 v[118:121], v189 offset:33792
	ds_read_b128 v[122:125], v189 offset:42496
	ds_read_b128 v[126:129], v170 offset:64
	ds_read_b128 v[130:133], v189 offset:33856
	ds_read_b128 v[134:137], v189 offset:42560
	ds_read_b128 v[138:141], v170 offset:128
	ds_read_b128 v[142:145], v226 offset:33920
	ds_read_b128 v[146:149], v226 offset:42624
	ds_read_b128 v[150:153], v170 offset:192
	ds_read_b128 v[154:157], v226 offset:33984
	ds_read_b128 v[158:161], v226 offset:42688
	s_waitcnt lgkmcnt(10)
	v_mfma_f32_16x16x32_bf16 v[118:121], v[118:121], v[114:117], 0
	v_and_b32_e32 v202, 64, v244
	v_xor_b32_e32 v190, 1, v244
	s_waitcnt lgkmcnt(9)
	v_mfma_f32_16x16x32_bf16 v[114:117], v[122:125], v[114:117], 0
	ds_read_b128 v[122:125], v170 offset:256
	ds_read_b128 v[162:165], v189 offset:34048
	ds_read_b128 v[166:169], v189 offset:42752
	s_waitcnt lgkmcnt(10)
	v_mfma_f32_16x16x32_bf16 v[118:121], v[130:133], v[126:129], v[118:121]
	s_waitcnt lgkmcnt(9)
	v_mfma_f32_16x16x32_bf16 v[114:117], v[134:137], v[126:129], v[114:117]
	ds_read_b128 v[126:129], v170 offset:320
	ds_read_b128 v[130:133], v189 offset:34112
	ds_read_b128 v[134:137], v189 offset:42816
	s_waitcnt lgkmcnt(10)
	v_mfma_f32_16x16x32_bf16 v[118:121], v[142:145], v[138:141], v[118:121]
	s_waitcnt lgkmcnt(9)
	v_mfma_f32_16x16x32_bf16 v[114:117], v[146:149], v[138:141], v[114:117]
	ds_read_b128 v[138:141], v170 offset:384
	ds_read_b128 v[142:145], v226 offset:34176
	ds_read_b128 v[146:149], v226 offset:42880
	s_waitcnt lgkmcnt(10)
	v_mfma_f32_16x16x32_bf16 v[118:121], v[154:157], v[150:153], v[118:121]
	s_waitcnt lgkmcnt(9)
	v_mfma_f32_16x16x32_bf16 v[114:117], v[158:161], v[150:153], v[114:117]
	ds_read_b128 v[150:153], v170 offset:448
	ds_read_b128 v[154:157], v226 offset:34240
	ds_read_b128 v[158:161], v226 offset:42944
	s_waitcnt lgkmcnt(10)
	v_mfma_f32_16x16x32_bf16 v[118:121], v[162:165], v[122:125], v[118:121]
	v_cvt_pk_bf16_f32 v162, v94, v95
	s_waitcnt lgkmcnt(9)
	v_mfma_f32_16x16x32_bf16 v[114:117], v[166:169], v[122:125], v[114:117]
	v_cvt_pk_bf16_f32 v163, v96, v97
	v_cvt_pk_bf16_f32 v164, v90, v91
	v_cvt_pk_bf16_f32 v165, v92, v93
	s_waitcnt lgkmcnt(7)
	v_mfma_f32_16x16x32_bf16 v[118:121], v[130:133], v[126:129], v[118:121]
	v_add_u32_e32 v166, v225, v224
	s_waitcnt lgkmcnt(6)
	v_mfma_f32_16x16x32_bf16 v[114:117], v[134:137], v[126:129], v[114:117]
	s_waitcnt lgkmcnt(4)
	v_mfma_f32_16x16x32_bf16 v[118:121], v[142:145], v[138:141], v[118:121]
	s_waitcnt lgkmcnt(3)
	v_mfma_f32_16x16x32_bf16 v[114:117], v[146:149], v[138:141], v[114:117]
	v_cvt_pk_bf16_f32 v146, v102, v103
	v_cvt_pk_bf16_f32 v147, v104, v105
	v_cvt_pk_bf16_f32 v148, v98, v99
	s_waitcnt lgkmcnt(1)
	v_mfma_f32_16x16x32_bf16 v[118:121], v[154:157], v[150:153], v[118:121]
	v_cvt_pk_bf16_f32 v149, v100, v101
	s_waitcnt lgkmcnt(0)
	v_mfma_f32_16x16x32_bf16 v[114:117], v[158:161], v[150:153], v[114:117]
	s_nop 4
	v_cndmask_b32_e64 v118, v118, 0, s[10:11]
	v_cndmask_b32_e64 v119, 0, v119, s[12:13]
	s_nop 0
	v_cndmask_b32_e64 v114, v114, 0, s[18:19]
	v_cndmask_b32_e64 v115, v115, 0, s[20:21]
	v_cvt_pk_bf16_f32 v118, v118, v119
	v_cndmask_b32_e64 v119, v120, 0, s[14:15]
	v_cndmask_b32_e64 v120, v121, 0, s[16:17]
	v_cvt_pk_bf16_f32 v114, v114, v115
	v_cndmask_b32_e64 v115, v116, 0, s[22:23]
	v_cndmask_b32_e64 v116, v117, 0, s[24:25]
	v_cvt_pk_bf16_f32 v119, v119, v120
	v_cvt_pk_bf16_f32 v115, v115, v116
	ds_write_b64 v227, v[118:119]
	ds_write_b64 v228, v[114:115]
	ds_read_b64 v[126:127], v223
	ds_read_b64 v[128:129], v246
	ds_read_b64 v[130:131], v223 offset:8448
	ds_read_b64 v[132:133], v246 offset:8448
	ds_read_b64 v[134:135], v223 offset:16896
	ds_read_b64 v[136:137], v246 offset:16896
	ds_read_b64 v[138:139], v223 offset:25344
	ds_read_b64 v[140:141], v246 offset:25344
	ds_read_b64 v[142:143], v223 offset:64
	ds_read_b64 v[144:145], v246 offset:64
	ds_read_b64 v[122:123], v223 offset:8512
	ds_read_b64 v[124:125], v246 offset:8512
	ds_read_b64 v[114:115], v223 offset:16960
	ds_read_b64 v[116:117], v246 offset:16960
	ds_read_b64 v[118:119], v223 offset:25408
	ds_read_b64 v[120:121], v246 offset:25408
	s_waitcnt lgkmcnt(14)
	v_mfma_f32_16x16x32_bf16 v[126:129], v[146:149], v[126:129], 0
	s_waitcnt lgkmcnt(12)
	v_mfma_f32_16x16x32_bf16 v[130:133], v[146:149], v[130:133], 0
	s_waitcnt lgkmcnt(10)
	v_mfma_f32_16x16x32_bf16 v[134:137], v[146:149], v[134:137], 0
	s_waitcnt lgkmcnt(8)
	v_mfma_f32_16x16x32_bf16 v[138:141], v[146:149], v[138:141], 0
	ds_read_b64 v[146:147], v223 offset:128
	ds_read_b64 v[148:149], v246 offset:128
	ds_read_b64 v[150:151], v223 offset:8576
	ds_read_b64 v[152:153], v246 offset:8576
	ds_read_b64 v[154:155], v223 offset:17024
	ds_read_b64 v[156:157], v246 offset:17024
	ds_read_b64 v[158:159], v223 offset:25472
	ds_read_b64 v[160:161], v246 offset:25472
	s_waitcnt lgkmcnt(14)
	v_mfma_f32_16x16x32_bf16 v[126:129], v[162:165], v[142:145], v[126:129]
	s_waitcnt lgkmcnt(12)
	v_mfma_f32_16x16x32_bf16 v[122:125], v[162:165], v[122:125], v[130:133]
	s_waitcnt lgkmcnt(10)
	v_mfma_f32_16x16x32_bf16 v[114:117], v[162:165], v[114:117], v[134:137]
	s_waitcnt lgkmcnt(8)
; __device__ __forceinline__ unsigned cvtpk(float lo, float hi) { f32x2_t v = {lo, hi}; bf16x2_t b = __builtin_convertvector(v, bf16x2_t); return __builtin_bit_cast(unsigned, b); }
; #define GLA_FENCE() asm volatile("" ::: "memory")
; #define GLA_BAR() do { asm volatile("s_waitcnt lgkmcnt(0)" ::: "memory"); __builtin_amdgcn_s_barrier(); asm volatile("" ::: "memory"); } while (0)
; #define Q_LOAD(sl, ks) do { _Pragma("unroll") for (int i4 = 0; i4 < 4; ++i4) qa[sl][i4] = cat4(*(const LAS s16x4*)(qperm + i4 * 16 * QS + (ks) * 64), *(const LAS s16x4*)(qperm2 + i4 * 16 * QS + (ks) * 64)); } while (0)
; template <int PASS> ...
;     ...
;             bf16x8 qa[2][4];
;     ...
;             Q_LOAD(0, 0); GLA_FENCE();
; #pragma unroll
;             for (int ks = 0; ks < 8; ++ks) {
;                 if (ks + 1 < 8) Q_LOAD((ks + 1) & 1, ks + 1);
;                 GLA_FENCE();
;                 v4u bw; bw.x = cvtpk(S[2 * ks][0], S[2 * ks][1]); bw.y = cvtpk(S[2 * ks][2], S[2 * ks][3]); bw.z = cvtpk(S[2 * ks + 1][0], S[2 * ks + 1][1]); bw.w = cvtpk(S[2 * ks + 1][2], S[2 * ks + 1][3]);
;                 const bf16x8 bfrag = __builtin_bit_cast(bf16x8, bw);
; #pragma unroll
;                 for (int i4 = 0; i4 < 4; ++i4) Oa[i4] = __builtin_amdgcn_mfma_f32_16x16x32_bf16(bfrag, qa[ks & 1][i4], Oa[i4], 0, 0, 0);
;             }
;     ...
;             GLA_BAR();
	v_mfma_f32_16x16x32_bf16 v[118:121], v[162:165], v[118:121], v[138:141]
	v_cvt_pk_bf16_f32 v162, v70, v71
	v_cvt_pk_bf16_f32 v163, v72, v73
	v_cvt_pk_bf16_f32 v164, v54, v55
	v_cvt_pk_bf16_f32 v165, v56, v57
	ds_read_b64 v[130:131], v223 offset:192
	ds_read_b64 v[132:133], v246 offset:192
	ds_read_b64 v[134:135], v223 offset:8640
	ds_read_b64 v[136:137], v246 offset:8640
	ds_read_b64 v[138:139], v223 offset:17088
	ds_read_b64 v[140:141], v246 offset:17088
	ds_read_b64 v[142:143], v223 offset:25536
	ds_read_b64 v[144:145], v246 offset:25536
	s_waitcnt lgkmcnt(14)
	v_mfma_f32_16x16x32_bf16 v[126:129], v[162:165], v[146:149], v[126:129]
	s_waitcnt lgkmcnt(12)
	v_mfma_f32_16x16x32_bf16 v[122:125], v[162:165], v[150:153], v[122:125]
	s_waitcnt lgkmcnt(10)
	v_mfma_f32_16x16x32_bf16 v[114:117], v[162:165], v[154:157], v[114:117]
	s_waitcnt lgkmcnt(8)
	v_mfma_f32_16x16x32_bf16 v[118:121], v[162:165], v[158:161], v[118:121]
	v_cvt_pk_bf16_f32 v162, v38, v39
	v_cvt_pk_bf16_f32 v163, v40, v41
	v_cvt_pk_bf16_f32 v164, v34, v35
	v_cvt_pk_bf16_f32 v165, v36, v37
	ds_read_b64 v[146:147], v223 offset:256
	ds_read_b64 v[148:149], v246 offset:256
	ds_read_b64 v[150:151], v223 offset:8704
	ds_read_b64 v[152:153], v246 offset:8704
	ds_read_b64 v[154:155], v223 offset:17152
	ds_read_b64 v[156:157], v246 offset:17152
	ds_read_b64 v[158:159], v223 offset:25600
	ds_read_b64 v[160:161], v246 offset:25600
	s_waitcnt lgkmcnt(14)
	v_mfma_f32_16x16x32_bf16 v[126:129], v[162:165], v[130:133], v[126:129]
	s_waitcnt lgkmcnt(12)
	v_mfma_f32_16x16x32_bf16 v[122:125], v[162:165], v[134:137], v[122:125]
	s_waitcnt lgkmcnt(10)
	v_mfma_f32_16x16x32_bf16 v[114:117], v[162:165], v[138:141], v[114:117]
	s_waitcnt lgkmcnt(8)
	v_mfma_f32_16x16x32_bf16 v[118:121], v[162:165], v[142:145], v[118:121]
	v_cvt_pk_bf16_f32 v162, v30, v31
	v_cvt_pk_bf16_f32 v163, v32, v33
	v_cvt_pk_bf16_f32 v164, v26, v27
	v_cvt_pk_bf16_f32 v165, v28, v29
	ds_read_b64 v[130:131], v223 offset:320
	ds_read_b64 v[132:133], v246 offset:320
	ds_read_b64 v[134:135], v223 offset:8768
	ds_read_b64 v[136:137], v246 offset:8768
	ds_read_b64 v[138:139], v223 offset:17216
	ds_read_b64 v[140:141], v246 offset:17216
	ds_read_b64 v[142:143], v223 offset:25664
	ds_read_b64 v[144:145], v246 offset:25664
	s_waitcnt lgkmcnt(14)
	v_mfma_f32_16x16x32_bf16 v[126:129], v[162:165], v[146:149], v[126:129]
	s_waitcnt lgkmcnt(12)
	v_mfma_f32_16x16x32_bf16 v[122:125], v[162:165], v[150:153], v[122:125]
	s_waitcnt lgkmcnt(10)
	v_mfma_f32_16x16x32_bf16 v[114:117], v[162:165], v[154:157], v[114:117]
	s_waitcnt lgkmcnt(8)
	v_mfma_f32_16x16x32_bf16 v[118:121], v[162:165], v[158:161], v[118:121]
	v_cvt_pk_bf16_f32 v162, v22, v23
	v_cvt_pk_bf16_f32 v163, v24, v25
	v_cvt_pk_bf16_f32 v164, v18, v19
	v_cvt_pk_bf16_f32 v165, v20, v21
	ds_read_b64 v[146:147], v223 offset:384
	ds_read_b64 v[148:149], v246 offset:384
	ds_read_b64 v[150:151], v223 offset:8832
	ds_read_b64 v[152:153], v246 offset:8832
	ds_read_b64 v[154:155], v223 offset:17280
	ds_read_b64 v[156:157], v246 offset:17280
	ds_read_b64 v[158:159], v223 offset:25728
	ds_read_b64 v[160:161], v246 offset:25728
	s_waitcnt lgkmcnt(14)
	v_mfma_f32_16x16x32_bf16 v[126:129], v[162:165], v[130:133], v[126:129]
	s_waitcnt lgkmcnt(12)
	v_mfma_f32_16x16x32_bf16 v[122:125], v[162:165], v[134:137], v[122:125]
	s_waitcnt lgkmcnt(10)
	v_mfma_f32_16x16x32_bf16 v[114:117], v[162:165], v[138:141], v[114:117]
	s_waitcnt lgkmcnt(8)
	v_mfma_f32_16x16x32_bf16 v[118:121], v[162:165], v[142:145], v[118:121]
	v_cvt_pk_bf16_f32 v162, v14, v15
	v_cvt_pk_bf16_f32 v163, v16, v17
	v_cvt_pk_bf16_f32 v164, v10, v11
	v_cvt_pk_bf16_f32 v165, v12, v13
	ds_read_b64 v[130:131], v223 offset:448
	ds_read_b64 v[132:133], v246 offset:448
	ds_read_b64 v[134:135], v223 offset:8896
	ds_read_b64 v[136:137], v246 offset:8896
	ds_read_b64 v[138:139], v223 offset:17344
	ds_read_b64 v[140:141], v246 offset:17344
	ds_read_b64 v[142:143], v223 offset:25792
	ds_read_b64 v[144:145], v246 offset:25792
	s_waitcnt lgkmcnt(14)
	v_mfma_f32_16x16x32_bf16 v[126:129], v[162:165], v[146:149], v[126:129]
	v_cvt_pk_bf16_f32 v146, v6, v7
	v_cvt_pk_bf16_f32 v147, v8, v9
	v_cvt_pk_bf16_f32 v148, v2, v3
	v_cvt_pk_bf16_f32 v149, v4, v5
	s_waitcnt lgkmcnt(12)
	v_mfma_f32_16x16x32_bf16 v[122:125], v[162:165], v[150:153], v[122:125]
	s_waitcnt lgkmcnt(0)
	s_waitcnt lgkmcnt(10)
	v_mfma_f32_16x16x32_bf16 v[114:117], v[162:165], v[154:157], v[114:117]
	s_barrier
; #define GAS __attribute__((address_space(1)))
; #define LAS __attribute__((address_space(3)))
; __device__ __forceinline__ unsigned cvtpk(float lo, float hi) { f32x2_t v = {lo, hi}; bf16x2_t b = __builtin_convertvector(v, bf16x2_t); return __builtin_bit_cast(unsigned, b); }
; #define GTP_BEGIN(k) do { if ((TPROBE_MASK >> (k)) & 1u) { if (tid == 0) ((volatile LAS int*)(lds + MISC_OFF))[50] = (int)__builtin_amdgcn_s_memrealtime(); } } while (0)
; #define GLA_FENCE() asm volatile("" ::: "memory")
; template <int PASS> ...
;     ...
; #pragma unroll
;             for (int i = 0; i < 2; ++i) gpre[i] = *(const GAS v4u*)((const GAS char*)GB + (size_t)tok0 * VD * 2 + i * 32 * VD * 2 + voff);
;             { bf16x8 pf[6];
;               pf[0] = *(const LAS bf16x8*)(pnat); pf[1] = *(const LAS bf16x8*)(pnat + 16 * PS); pf[2] = *(const LAS bf16x8*)(pnat + 32 * PS); pf[3] = *(const LAS bf16x8*)(pnat + 32 * PS + 64);
;               pf[4] = *(const LAS bf16x8*)(pnat + 48 * PS); pf[5] = *(const LAS bf16x8*)(pnat + 48 * PS + 64);
;               Oa[0] = __builtin_amdgcn_mfma_f32_16x16x32_bf16(vb[0], pf[0], Oa[0], 0, 0, 0); Oa[1] = __builtin_amdgcn_mfma_f32_16x16x32_bf16(vb[0], pf[1], Oa[1], 0, 0, 0);
;               Oa[2] = __builtin_amdgcn_mfma_f32_16x16x32_bf16(vb[0], pf[2], Oa[2], 0, 0, 0); Oa[2] = __builtin_amdgcn_mfma_f32_16x16x32_bf16(vb[1], pf[3], Oa[2], 0, 0, 0);
;               Oa[3] = __builtin_amdgcn_mfma_f32_16x16x32_bf16(vb[0], pf[4], Oa[3], 0, 0, 0); Oa[3] = __builtin_amdgcn_mfma_f32_16x16x32_bf16(vb[1], pf[5], Oa[3], 0, 0, 0); }
; #pragma unroll
;             for (int i4 = 0; i4 < 4; ++i4) { v2u o; o.x = cvtpk(Oa[i4][0], Oa[i4][1]); o.y = cvtpk(Oa[i4][2], Oa[i4][3]); *(LAS v2u*)(lds + OFF_O + (16 * i4 + r) * OS + (16 * w + 4 * q) * 2) = o; }
;         }
;         if (PASS == 2) { GTP_END(25); GTP_BEGIN(26); }
;         { constexpr int RD = (PASS == 1) ? 4 : 2;
;           bf16x8 ka0[RD], ka1[RD]; f32x4 gg[RD];
;     ...
; #pragma unroll
;           for (int d0 = 0; d0 < RD - 1; ++d0) KV_LOAD(d0, d0);
; #pragma unroll
;           for (int dt = 0; dt < 16; ++dt) { if (dt + RD - 1 < 16) KV_LOAD((dt + RD - 1) % RD, dt + RD - 1); GLA_FENCE();
;               S[dt] = __builtin_amdgcn_mfma_f32_16x16x32_bf16(ka0[dt % RD], vb[0], S[dt], 0, 0, 0); S[dt] = __builtin_amdgcn_mfma_f32_16x16x32_bf16(ka1[dt % RD], vb[1], S[dt], 0, 0, 0);
;               S[dt] = S[dt] * gg[dt % RD]; }
	s_waitcnt lgkmcnt(8)
	v_mfma_f32_16x16x32_bf16 v[118:121], v[162:165], v[158:161], v[118:121]
	s_waitcnt lgkmcnt(6)
	v_mfma_f32_16x16x32_bf16 v[130:133], v[146:149], v[130:133], v[126:129]
	s_nop 2
	v_add_co_u32_e32 v126, vcc, s88, v208
	s_waitcnt lgkmcnt(4)
	v_mfma_f32_16x16x32_bf16 v[122:125], v[146:149], v[134:137], v[122:125]
	v_addc_co_u32_e32 v127, vcc, -1, v209, vcc
	s_waitcnt lgkmcnt(2)
	v_mfma_f32_16x16x32_bf16 v[114:117], v[146:149], v[138:141], v[114:117]
	s_waitcnt lgkmcnt(0)
	v_mfma_f32_16x16x32_bf16 v[118:121], v[146:149], v[142:145], v[118:121]
	global_load_dwordx4 v[146:149], v[126:127], off
	v_add_co_u32_e32 v126, vcc, s89, v208
	s_nop 1
	v_addc_co_u32_e32 v127, vcc, -1, v209, vcc
	global_load_dwordx4 v[126:129], v[126:127], off
	ds_read_b128 v[134:137], v229
	ds_read_b128 v[138:141], v229 offset:2304
	ds_read_b128 v[142:145], v229 offset:4608
	ds_read_b128 v[150:153], v229 offset:4672
	ds_read_b128 v[154:157], v229 offset:6912
	ds_read_b128 v[158:161], v229 offset:6976
	s_waitcnt lgkmcnt(3)
	v_mfma_f32_16x16x32_bf16 v[114:117], v[106:109], v[142:145], v[114:117]
	s_waitcnt lgkmcnt(1)
	v_mfma_f32_16x16x32_bf16 v[118:121], v[106:109], v[154:157], v[118:121]
	v_mfma_f32_16x16x32_bf16 v[114:117], v[110:113], v[150:153], v[114:117]
	v_mfma_f32_16x16x32_bf16 v[130:133], v[106:109], v[134:137], v[130:133]
	v_mfma_f32_16x16x32_bf16 v[122:125], v[106:109], v[138:141], v[122:125]
	s_nop 5
	v_cvt_pk_bf16_f32 v114, v114, v115
	v_cvt_pk_bf16_f32 v115, v116, v117
	v_cvt_pk_bf16_f32 v130, v130, v131
	s_waitcnt lgkmcnt(0)
	v_mfma_f32_16x16x32_bf16 v[118:121], v[110:113], v[158:161], v[118:121]
	v_cvt_pk_bf16_f32 v131, v132, v133
	v_cvt_pk_bf16_f32 v122, v122, v123
	v_cvt_pk_bf16_f32 v123, v124, v125
	ds_write_b64 v230, v[114:115] offset:8704
	ds_write_b64 v230, v[130:131]
	s_nop 2
	v_cvt_pk_bf16_f32 v114, v118, v119
	v_cvt_pk_bf16_f32 v115, v120, v121
	ds_write_b64 v230, v[122:123] offset:4352
	ds_write_b64 v230, v[114:115] offset:13056
	ds_read_b64_tr_b16 v[124:125], v166 offset:35968
	ds_read_b64_tr_b16 v[130:131], v166 offset:51200
	ds_read_b64_tr_b16 v[132:133], v166 offset:53376
	ds_read_b64_tr_b16 v[122:123], v166 offset:33792
	ds_read_b64_tr_b16 v[134:135], v166 offset:33824
	v_add_u32_e32 v114, 0, v221
	v_add_u32_e32 v182, 0x17800, v114
	ds_read_b128 v[114:117], v182
	ds_read_b64_tr_b16 v[136:137], v166 offset:36000
	ds_read_b64_tr_b16 v[138:139], v166 offset:51232
	ds_read_b64_tr_b16 v[140:141], v166 offset:53408
	ds_read_b128 v[118:121], v182 offset:64
	s_waitcnt lgkmcnt(6)
	v_mfma_f32_16x16x32_bf16 v[102:105], v[122:125], v[106:109], v[102:105]
	ds_read_b64_tr_b16 v[142:143], v166 offset:33856
	ds_read_b64_tr_b16 v[144:145], v166 offset:36032
	ds_read_b64_tr_b16 v[150:151], v166 offset:51264
	ds_read_b64_tr_b16 v[152:153], v166 offset:53440
	ds_read_b128 v[122:125], v182 offset:128
	s_waitcnt lgkmcnt(8)
	v_mfma_f32_16x16x32_bf16 v[98:101], v[134:137], v[106:109], v[98:101]
	v_mfma_f32_16x16x32_bf16 v[102:105], v[130:133], v[110:113], v[102:105]
	s_waitcnt lgkmcnt(6)
	v_mfma_f32_16x16x32_bf16 v[98:101], v[138:141], v[110:113], v[98:101]
	ds_read_b64_tr_b16 v[138:139], v166 offset:33888
	ds_read_b64_tr_b16 v[140:141], v166 offset:36064
	ds_read_b64_tr_b16 v[154:155], v166 offset:51296
	ds_read_b64_tr_b16 v[156:157], v166 offset:53472
	ds_read_b128 v[130:133], v182 offset:192
	s_waitcnt lgkmcnt(8)
	v_mfma_f32_16x16x32_bf16 v[94:97], v[142:145], v[106:109], v[94:97]
	s_waitcnt lgkmcnt(3)
	v_mfma_f32_16x16x32_bf16 v[90:93], v[138:141], v[106:109], v[90:93]
	v_mfma_f32_16x16x32_bf16 v[94:97], v[150:153], v[110:113], v[94:97]
	ds_read_b64_tr_b16 v[142:143], v231 offset:33920
	ds_read_b64_tr_b16 v[144:145], v231 offset:36096
	ds_read_b64_tr_b16 v[150:151], v231 offset:51328
	ds_read_b64_tr_b16 v[152:153], v231 offset:53504
	ds_read_b128 v[134:137], v182 offset:256
	s_waitcnt lgkmcnt(6)
	v_mfma_f32_16x16x32_bf16 v[90:93], v[154:157], v[110:113], v[90:93]
	ds_read_b64_tr_b16 v[154:155], v231 offset:33952
	ds_read_b64_tr_b16 v[156:157], v231 offset:36128
	ds_read_b64_tr_b16 v[158:159], v231 offset:51360
	ds_read_b64_tr_b16 v[160:161], v231 offset:53536
	ds_read_b128 v[138:141], v182 offset:320
	s_waitcnt lgkmcnt(8)
	v_mfma_f32_16x16x32_bf16 v[70:73], v[142:145], v[106:109], v[70:73]
	ds_read_b64_tr_b16 v[162:163], v231 offset:33984
	ds_read_b64_tr_b16 v[164:165], v231 offset:36160
	ds_read_b64_tr_b16 v[168:169], v231 offset:51392
	ds_read_b64_tr_b16 v[170:171], v231 offset:53568
	ds_read_b128 v[142:145], v182 offset:384
	s_waitcnt lgkmcnt(8)
	v_mfma_f32_16x16x32_bf16 v[54:57], v[154:157], v[106:109], v[54:57]
	v_mfma_f32_16x16x32_bf16 v[70:73], v[150:153], v[110:113], v[70:73]
	s_waitcnt lgkmcnt(6)
	v_mfma_f32_16x16x32_bf16 v[54:57], v[158:161], v[110:113], v[54:57]
	ds_read_b64_tr_b16 v[158:159], v231 offset:34016
	ds_read_b64_tr_b16 v[160:161], v231 offset:36192
	ds_read_b64_tr_b16 v[172:173], v231 offset:51424
	ds_read_b64_tr_b16 v[174:175], v231 offset:53600
	ds_read_b128 v[150:153], v182 offset:448
	s_waitcnt lgkmcnt(8)
	v_mfma_f32_16x16x32_bf16 v[38:41], v[162:165], v[106:109], v[38:41]
	s_waitcnt lgkmcnt(3)
; #define LAS __attribute__((address_space(3)))
; __device__ __forceinline__ f32x4 bf4lo(const v4u& w) { return (f32x4){bflo(w.x), bfhi(w.x), bflo(w.y), bfhi(w.y)}; }
; __device__ __forceinline__ f32x4 bf4hi(const v4u& w) { return (f32x4){bflo(w.z), bfhi(w.z), bflo(w.w), bfhi(w.w)}; }
; #define GTP_BEGIN(k) do { if ((TPROBE_MASK >> (k)) & 1u) { if (tid == 0) ((volatile LAS int*)(lds + MISC_OFF))[50] = (int)__builtin_amdgcn_s_memrealtime(); } } while (0)
; #define GTP_END(k) do { if ((TPROBE_MASK >> (k)) & 1u) { if (tid == 0) { volatile LAS int* m_ = (volatile LAS int*)(lds + MISC_OFF); m_[51] = m_[51] + ((int)__builtin_amdgcn_s_memrealtime() - m_[50]); } } } while (0)
; #define GLA_FENCE() asm volatile("" ::: "memory")
; #define GLA_BAR() do { asm volatile("s_waitcnt lgkmcnt(0)" ::: "memory"); __builtin_amdgcn_s_barrier(); asm volatile("" ::: "memory"); } while (0)
; template <int PASS> ...
;     ...
; #pragma unroll
;           for (int d0 = 0; d0 < RD - 1; ++d0) KV_LOAD(d0, d0);
; #pragma unroll
;           for (int dt = 0; dt < 16; ++dt) { if (dt + RD - 1 < 16) KV_LOAD((dt + RD - 1) % RD, dt + RD - 1); GLA_FENCE();
;               S[dt] = __builtin_amdgcn_mfma_f32_16x16x32_bf16(ka0[dt % RD], vb[0], S[dt], 0, 0, 0); S[dt] = __builtin_amdgcn_mfma_f32_16x16x32_bf16(ka1[dt % RD], vb[1], S[dt], 0, 0, 0);
;               S[dt] = S[dt] * gg[dt % RD]; }
;     ...
;         }
;         if (PASS == 2) { GTP_END(26); GTP_BEGIN(27); }
;         GLA_BAR();
;         if (PASS == 2) {
;             const f32x4 hw0 = *(const LAS f32x4*)(lds + MISC_OFF + 256 + (tid & 15) * 32), hw1 = *(const LAS f32x4*)(lds + MISC_OFF + 256 + (tid & 15) * 32 + 16);
; #pragma unroll
;             for (int i = 0; i < 2; ++i) { const int id = tid + 512 * i, row = id >> 4, cc = id & 15;
;                 const v4u ov = *(const LAS v4u*)(lds + OFF_O + row * OS + cc * 16);
;                 const f32x4 a = bf4lo(ov), b = bf4hi(ov), ga = bf4lo(gpre[i]), gb = bf4hi(gpre[i]);
;                 float ss = (a.x * a.x + a.y * a.y) + (a.z * a.z + a.w * a.w) + (b.x * b.x + b.y * b.y) + (b.z * b.z + b.w * b.w);
;                 ss += __shfl_xor(ss, 1); ss += __shfl_xor(ss, 2); ss += __shfl_xor(ss, 4); ss += __shfl_xor(ss, 8);
;                 if (cc == 0) SS[(size_t)(tok0 + row) * 16 + h * 4 + s] = ss;
	v_mfma_f32_16x16x32_bf16 v[34:37], v[158:161], v[106:109], v[34:37]
	v_mfma_f32_16x16x32_bf16 v[38:41], v[168:171], v[110:113], v[38:41]
	ds_read_b64_tr_b16 v[162:163], v166 offset:34048
	ds_read_b64_tr_b16 v[164:165], v166 offset:36224
	ds_read_b64_tr_b16 v[168:169], v166 offset:51456
	ds_read_b64_tr_b16 v[170:171], v166 offset:53632
	ds_read_b128 v[154:157], v182 offset:512
	s_waitcnt lgkmcnt(6)
	v_mfma_f32_16x16x32_bf16 v[34:37], v[172:175], v[110:113], v[34:37]
	ds_read_b64_tr_b16 v[172:173], v166 offset:34080
	ds_read_b64_tr_b16 v[174:175], v166 offset:36256
	ds_read_b64_tr_b16 v[176:177], v166 offset:51488
	ds_read_b64_tr_b16 v[178:179], v166 offset:53664
	ds_read_b128 v[158:161], v182 offset:576
	s_waitcnt lgkmcnt(8)
	v_mfma_f32_16x16x32_bf16 v[30:33], v[162:165], v[106:109], v[30:33]
	ds_read_b64_tr_b16 v[210:211], v166 offset:34112
	ds_read_b64_tr_b16 v[212:213], v166 offset:36288
	ds_read_b64_tr_b16 v[214:215], v166 offset:51520
	ds_read_b64_tr_b16 v[216:217], v166 offset:53696
	ds_read_b128 v[162:165], v182 offset:640
	s_waitcnt lgkmcnt(8)
	v_mfma_f32_16x16x32_bf16 v[26:29], v[172:175], v[106:109], v[26:29]
	s_waitcnt lgkmcnt(3)
	v_mfma_f32_16x16x32_bf16 v[22:25], v[210:213], v[106:109], v[22:25]
	v_mfma_f32_16x16x32_bf16 v[30:33], v[168:171], v[110:113], v[30:33]
	v_mfma_f32_16x16x32_bf16 v[26:29], v[176:179], v[110:113], v[26:29]
	ds_read_b64_tr_b16 v[174:175], v166 offset:34144
	ds_read_b64_tr_b16 v[176:177], v166 offset:36320
	ds_read_b64_tr_b16 v[178:179], v166 offset:51552
	ds_read_b64_tr_b16 v[180:181], v166 offset:53728
	ds_read_b128 v[166:169], v182 offset:704
	s_waitcnt lgkmcnt(6)
	v_mfma_f32_16x16x32_bf16 v[22:25], v[214:217], v[110:113], v[22:25]
	ds_read_b64_tr_b16 v[210:211], v231 offset:34176
	ds_read_b64_tr_b16 v[212:213], v231 offset:36352
	ds_read_b64_tr_b16 v[214:215], v231 offset:51584
	ds_read_b64_tr_b16 v[216:217], v231 offset:53760
	ds_read_b128 v[170:173], v182 offset:768
	s_waitcnt lgkmcnt(8)
	v_mfma_f32_16x16x32_bf16 v[18:21], v[174:177], v[106:109], v[18:21]
	ds_read_b64_tr_b16 v[248:249], v231 offset:34208
	ds_read_b64_tr_b16 v[250:251], v231 offset:36384
	ds_read_b64_tr_b16 v[252:253], v231 offset:51616
	ds_read_b64_tr_b16 v[254:255], v231 offset:53792
	ds_read_b128 v[174:177], v182 offset:832
	s_waitcnt lgkmcnt(8)
	v_mfma_f32_16x16x32_bf16 v[14:17], v[210:213], v[106:109], v[14:17]
	s_waitcnt lgkmcnt(3)
	v_mfma_f32_16x16x32_bf16 v[10:13], v[248:251], v[106:109], v[10:13]
	v_mfma_f32_16x16x32_bf16 v[18:21], v[178:181], v[110:113], v[18:21]
	v_mfma_f32_16x16x32_bf16 v[14:17], v[214:217], v[110:113], v[14:17]
	ds_read_b64_tr_b16 v[210:211], v231 offset:34240
	ds_read_b64_tr_b16 v[212:213], v231 offset:36416
	ds_read_b64_tr_b16 v[214:215], v231 offset:51648
	ds_read_b64_tr_b16 v[216:217], v231 offset:53824
	ds_read_b128 v[178:181], v182 offset:896
	s_waitcnt lgkmcnt(6)
	v_mfma_f32_16x16x32_bf16 v[10:13], v[252:255], v[110:113], v[10:13]
	ds_read_b64_tr_b16 v[248:249], v231 offset:34272
	ds_read_b64_tr_b16 v[250:251], v231 offset:36448
	ds_read_b64_tr_b16 v[252:253], v231 offset:51680
	ds_read_b64_tr_b16 v[254:255], v231 offset:53856
	ds_read_b128 v[182:185], v182 offset:960
	s_waitcnt lgkmcnt(8)
	v_mfma_f32_16x16x32_bf16 v[6:9], v[210:213], v[106:109], v[6:9]
	v_add_u32_e32 v210, 64, v202
	s_waitcnt lgkmcnt(0)
	s_barrier
	s_waitcnt lgkmcnt(3)
	v_mfma_f32_16x16x32_bf16 v[2:5], v[248:251], v[106:109], v[2:5]
	v_cmp_lt_i32_e32 vcc, v190, v210
	v_mfma_f32_16x16x32_bf16 v[6:9], v[214:217], v[110:113], v[6:9]
	s_nop 0
	v_cndmask_b32_e32 v190, v244, v190, vcc
	v_lshlrev_b32_e32 v249, 2, v190
	v_xor_b32_e32 v190, 2, v244
	s_waitcnt lgkmcnt(1)
	v_mfma_f32_16x16x32_bf16 v[2:5], v[252:255], v[110:113], v[2:5]
	ds_read_b128 v[110:113], v232
	ds_read_b128 v[106:109], v232 offset:16
	ds_read_b128 v[250:253], v233
	v_cmp_lt_i32_e32 vcc, v190, v210
	s_waitcnt lgkmcnt(0)
	v_and_b32_e32 v213, 0xffff0000, v250
	v_cndmask_b32_e32 v190, v244, v190, vcc
	v_lshlrev_b32_e32 v248, 2, v190
	v_xor_b32_e32 v190, 4, v244
	v_cmp_lt_i32_e32 vcc, v190, v210
	v_and_b32_e32 v217, 0xffff0000, v251
	v_lshlrev_b32_e32 v212, 16, v250
	v_cndmask_b32_e32 v190, v244, v190, vcc
	v_lshlrev_b32_e32 v216, 16, v251
	v_mul_f32_e32 v250, v213, v213
	v_mul_f32_e32 v251, v217, v217
	v_lshlrev_b32_e32 v202, 2, v190
	v_xor_b32_e32 v190, 8, v244
	v_and_b32_e32 v211, 0xffff0000, v252
	v_fmac_f32_e32 v250, v212, v212
	v_fmac_f32_e32 v251, v216, v216
	v_cmp_lt_i32_e32 vcc, v190, v210
	v_lshlrev_b32_e32 v210, 16, v252
	v_add_f32_e32 v250, v250, v251
	v_mul_f32_e32 v251, v211, v211
	v_and_b32_e32 v215, 0xffff0000, v253
	v_fmac_f32_e32 v251, v210, v210
	v_lshlrev_b32_e32 v214, 16, v253
	v_add_f32_e32 v250, v251, v250
	v_mul_f32_e32 v251, v215, v215
	v_fmac_f32_e32 v251, v214, v214
	v_add_f32_e32 v250, v251, v250
	ds_bpermute_b32 v251, v249, v250
	v_cndmask_b32_e32 v190, v244, v190, vcc
	v_lshlrev_b32_e32 v190, 2, v190
	s_waitcnt lgkmcnt(0)
	v_add_f32_e32 v250, v250, v251
	ds_bpermute_b32 v251, v248, v250
	s_waitcnt lgkmcnt(0)
	v_add_f32_e32 v250, v250, v251
	ds_bpermute_b32 v251, v202, v250
	s_waitcnt lgkmcnt(0)
	v_add_f32_e32 v250, v250, v251
	ds_bpermute_b32 v251, v190, v250
	s_and_saveexec_b64 s[64:65], s[26:27]
	s_cbranch_execz .LBB0_426
	s_waitcnt lgkmcnt(0)
	v_add_f32_e32 v252, v250, v251
	v_add_u32_e32 v250, s60, v219
	v_add_u32_e32 v250, s50, v250
	v_ashrrev_i32_e32 v251, 31, v250
	v_lshlrev_b64 v[250:251], 6, v[250:251]
	v_lshl_add_u64 v[250:251], s[62:63], 0, v[250:251]
	global_store_dword v[250:251], v252, off
